# scan loop: 7 broadcast v_mov copies replaced by op_sel high-half selects (on top of log range-handling trim)
# baseline (speedup 1.0000x reference)
; __device__ __forceinline__ void p0_norm_gl(Frame& F) {
;     ...
;             const int c0 = F.tid, c1 = F.tid + 512; v2f wv[16];
; #pragma unroll
;             for (int r = 0; r < 16; ++r) wv[r] = (v2f){w2[r * KD + c0], w2[r * KD + c1]};
;             const v2f bv = (v2f){bgk[c0], bgk[c1]}; float cuma = 0.f, cumb = 0.f;
; #pragma unroll 2
;             for (int t = 0; t < CHK; ++t) {
;                 v2f z = bv;
; #pragma unroll
;                 for (int r = 0; r < 16; ++r) { const float g = glc[t * 16 + r]; z = __builtin_elementwise_fma(wv[r], (v2f){g, g}, z); }
;                 const float za = z.x, zb = z.y;
;                 const float la = fminf(za, 0.f) - __logf(1.0f + __expf(-fabsf(za))), lb = fminf(zb, 0.f) - __logf(1.0f + __expf(-fabsf(zb)));
;                 cuma += la * (1.0f / 16.0f); cumb += lb * (1.0f / 16.0f);
;                 BC[(size_t)(ch * CHK + t) * KD + c0] = cuma; BC[(size_t)(ch * CHK + t) * KD + c1] = cumb;
;             }
.LBB0_181:
	s_add_i32 s11, s45, 0
	v_mov_b32_e32 v144, s11
	ds_read_b128 v[38:41], v144 offset:34816
	ds_read_b128 v[42:45], v144 offset:34832
	ds_read_b128 v[46:49], v144 offset:34848
	ds_read_b128 v[50:53], v144 offset:34864
	ds_read_b128 v[54:57], v144 offset:34880
	ds_read_b128 v[58:61], v144 offset:34896
	ds_read_b128 v[62:65], v144 offset:34912
	ds_read_b128 v[144:147], v144 offset:34928
	s_waitcnt lgkmcnt(7)
	v_pk_fma_f32 v[162:163], v[2:3], v[38:39], v[34:35] op_sel_hi:[1,0,1]
	s_waitcnt lgkmcnt(3)
	v_pk_fma_f32 v[172:173], v[2:3], v[54:55], v[34:35] op_sel_hi:[1,0,1]
	v_pk_fma_f32 v[38:39], v[4:5], v[38:39], v[162:163] op_sel:[0,1,0]
	v_mov_b32_e32 v164, v41
	v_pk_fma_f32 v[54:55], v[4:5], v[54:55], v[172:173] op_sel:[0,1,0]
	v_pk_fma_f32 v[38:39], v[6:7], v[40:41], v[38:39] op_sel_hi:[1,0,1]
	v_pk_fma_f32 v[40:41], v[6:7], v[56:57], v[54:55] op_sel_hi:[1,0,1]
	v_pk_fma_f32 v[38:39], v[8:9], v[164:165], v[38:39] op_sel_hi:[1,0,1]
	v_pk_fma_f32 v[40:41], v[8:9], v[56:57], v[40:41] op_sel:[0,1,0]
	v_pk_fma_f32 v[38:39], v[10:11], v[42:43], v[38:39] op_sel_hi:[1,0,1]
	s_waitcnt lgkmcnt(2)
	v_pk_fma_f32 v[40:41], v[10:11], v[58:59], v[40:41] op_sel_hi:[1,0,1]
	v_pk_fma_f32 v[38:39], v[12:13], v[42:43], v[38:39] op_sel:[0,1,0]
	v_pk_fma_f32 v[40:41], v[12:13], v[58:59], v[40:41] op_sel:[0,1,0]
	v_pk_fma_f32 v[38:39], v[14:15], v[44:45], v[38:39] op_sel_hi:[1,0,1]
	v_pk_fma_f32 v[40:41], v[14:15], v[60:61], v[40:41] op_sel_hi:[1,0,1]
	v_pk_fma_f32 v[38:39], v[16:17], v[44:45], v[38:39] op_sel:[0,1,0]
	v_pk_fma_f32 v[40:41], v[16:17], v[60:61], v[40:41] op_sel:[0,1,0]
	v_pk_fma_f32 v[38:39], v[18:19], v[46:47], v[38:39] op_sel_hi:[1,0,1]
	s_waitcnt lgkmcnt(1)
	v_pk_fma_f32 v[40:41], v[18:19], v[62:63], v[40:41] op_sel_hi:[1,0,1]
	v_pk_fma_f32 v[38:39], v[20:21], v[46:47], v[38:39] op_sel:[0,1,0]
	v_pk_fma_f32 v[40:41], v[20:21], v[62:63], v[40:41] op_sel:[0,1,0]
	v_pk_fma_f32 v[38:39], v[22:23], v[48:49], v[38:39] op_sel_hi:[1,0,1]
	v_pk_fma_f32 v[40:41], v[22:23], v[64:65], v[40:41] op_sel_hi:[1,0,1]
	v_pk_fma_f32 v[38:39], v[24:25], v[48:49], v[38:39] op_sel:[0,1,0]
	v_pk_fma_f32 v[40:41], v[24:25], v[64:65], v[40:41] op_sel:[0,1,0]
	v_pk_fma_f32 v[38:39], v[26:27], v[50:51], v[38:39] op_sel_hi:[1,0,1]
	s_waitcnt lgkmcnt(0)
	v_pk_fma_f32 v[40:41], v[26:27], v[144:145], v[40:41] op_sel_hi:[1,0,1]
	v_pk_fma_f32 v[38:39], v[28:29], v[50:51], v[38:39] op_sel:[0,1,0]
	v_pk_fma_f32 v[40:41], v[28:29], v[144:145], v[40:41] op_sel:[0,1,0]
	v_pk_fma_f32 v[38:39], v[30:31], v[52:53], v[38:39] op_sel_hi:[1,0,1]
	v_pk_fma_f32 v[40:41], v[30:31], v[146:147], v[40:41] op_sel_hi:[1,0,1]
	v_pk_fma_f32 v[38:39], v[32:33], v[52:53], v[38:39] op_sel:[0,1,0]
	v_pk_fma_f32 v[40:41], v[32:33], v[146:147], v[40:41] op_sel:[0,1,0]
	v_mul_f32_e64 v44, |v38|, s59
	v_mul_f32_e64 v45, |v39|, s59
	v_min_f32_e32 v43, 0, v38
	v_min_f32_e32 v42, 0, v39
	v_min_f32_e32 v39, 0, v40
	v_mul_f32_e64 v40, |v40|, s59
	v_min_f32_e32 v38, 0, v41
	v_mul_f32_e64 v41, |v41|, s59
	v_exp_f32_e32 v44, v44
	v_exp_f32_e32 v45, v45
	v_exp_f32_e32 v40, v40
	v_exp_f32_e32 v41, v41
	s_add_i32 s10, s46, 1
	s_ashr_i32 s11, s10, 31
	s_ashr_i32 s47, s46, 31
	s_lshl_b64 s[10:11], s[10:11], 12
	v_add_f32_e32 v44, 1.0, v44
	v_add_f32_e32 v45, 1.0, v45
	s_lshl_b64 s[12:13], s[46:47], 12
	v_lshl_add_u64 v[160:161], v[136:137], 0, s[10:11]
	v_add_f32_e32 v40, 1.0, v40
	v_add_f32_e32 v41, 1.0, v41
	v_lshl_add_u64 v[148:149], v[136:137], 0, s[12:13]
	v_log_f32_e32 v44, v44
	v_log_f32_e32 v45, v45
	v_log_f32_e32 v40, v40
	v_log_f32_e32 v41, v41
	v_mul_f32_e32 v50, 0x3f317217, v44
	v_mul_f32_e32 v51, 0x3f317217, v45
	v_mul_f32_e32 v52, 0x3f317217, v40
	v_mul_f32_e32 v53, 0x3f317217, v41
	v_fma_f32 v50, v44, s61, -v50
	v_fma_f32 v51, v45, s61, -v51
	v_fma_f32 v52, v40, s61, -v52
	v_fma_f32 v53, v41, s61, -v53
	v_fmac_f32_e32 v50, 0x3377d1cf, v44
	v_fmac_f32_e32 v51, 0x3377d1cf, v45
	v_fmac_f32_e32 v52, 0x3377d1cf, v40
	v_fmac_f32_e32 v53, 0x3377d1cf, v41
	v_fmac_f32_e32 v50, 0x3f317217, v44
	v_fmac_f32_e32 v51, 0x3f317217, v45
	v_fmac_f32_e32 v52, 0x3f317217, v40
	v_fmac_f32_e32 v53, 0x3f317217, v41
	v_pk_add_f32 v[40:41], v[42:43], v[50:51] op_sel:[0,1] op_sel_hi:[1,0] neg_lo:[0,1] neg_hi:[0,1]
	s_addk_i32 s45, 0x80
	s_add_i32 s46, s46, 2
	v_pk_add_f32 v[38:39], v[38:39], v[52:53] op_sel:[0,1] op_sel_hi:[1,0] neg_lo:[0,1] neg_hi:[0,1]
	v_pk_fma_f32 v[36:37], v[40:41], s[42:43], v[36:37] op_sel_hi:[1,0,1]
	s_cmpk_lg_i32 s45, 0x1000
	global_store_dword v[148:149], v37, off
	global_store_dword v[148:149], v36, off offset:2048
	v_pk_fma_f32 v[36:37], v[38:39], s[42:43], v[36:37] op_sel_hi:[1,0,1]
	global_store_dword v[160:161], v37, off
	global_store_dword v[160:161], v36, off offset:2048
	s_cbranch_scc1 .LBB0_181
	s_add_i32 s44, s44, s34
	s_add_i32 s3, s3, s35
	v_lshl_add_u64 v[140:141], v[140:141], 0, s[24:25]
	s_cmpk_lt_i32 s44, 0x100
	v_lshl_add_u64 v[142:143], v[142:143], 0, s[26:27]
	s_barrier
	s_cbranch_scc1 .LBB0_166
